# rt1: router unit: the 16 A-chunk loads of the first K half requested together at the unit head (were 8 dependent pairs), on top of g1b
# baseline (speedup 1.0000x reference)
; #define LAS __attribute__((address_space(3)))
; __global__ void __launch_bounds__(512, 2) fwd(Args args) {
;     ...
;                     const bf16_t* xr = XB + (size_t)(t0 + wave * 16 + (lane & 15)) * DM + (lane >> 4) * 8;
; #pragma unroll
;                     for (int kb = 0; kb < 32; ++kb) a[kb] = *(const bf16x8*)(xr + kb * 32);
; #pragma unroll
;                     for (int kb = 0; kb < 16; ++kb) {
; #pragma unroll
;                         for (int n = 0; n < 3; ++n) { const LAS bf16x8* bp = (const LAS bf16x8*)(lds + ((kb * 3 + n) * 128 + lane) * 16);
;                             acc[n] = __builtin_amdgcn_mfma_f32_16x16x32_bf16(a[kb], bp[0], acc[n], 0, 0, 0); acc[n] = __builtin_amdgcn_mfma_f32_16x16x32_bf16(a[kb], bp[64], acc[n], 0, 0, 0); } }
.LBB0_1272:
	v_readlane_b32 s2, v254, 54
	v_readlane_b32 s3, v254, 55
	s_lshl_b32 s2, s2, 6
	s_lshl_b32 s3, s3, 8
	s_andn2_b64 vcc, exec, s[0:1]
	s_add_i32 s0, s2, s3
	s_cbranch_vccnz .LBB0_1274
	v_or_b32_e32 v0, s0, v99
	v_ashrrev_i32_e32 v1, 31, v0
	v_lshlrev_b64 v[0:1], 11, v[0:1]
	v_lshl_add_u64 v[0:1], v[20:21], 0, v[0:1]
	global_load_dwordx4 v[2:5], v[0:1], off
	global_load_dwordx4 v[6:9], v[0:1], off offset:64
	global_load_dwordx4 v[170:173], v[0:1], off offset:128
	global_load_dwordx4 v[174:177], v[0:1], off offset:192
	global_load_dwordx4 v[178:181], v[0:1], off offset:256
	global_load_dwordx4 v[184:187], v[0:1], off offset:320
	global_load_dwordx4 v[188:191], v[0:1], off offset:384
	global_load_dwordx4 v[202:205], v[0:1], off offset:448
	global_load_dwordx4 v[206:209], v[0:1], off offset:512
	global_load_dwordx4 v[214:217], v[0:1], off offset:576
	global_load_dwordx4 v[218:221], v[0:1], off offset:640
	global_load_dwordx4 v[222:225], v[0:1], off offset:704
	global_load_dwordx4 v[226:229], v[0:1], off offset:768
	global_load_dwordx4 v[232:235], v[0:1], off offset:832
	global_load_dwordx4 v[238:241], v[0:1], off offset:896
	global_load_dwordx4 v[242:245], v[0:1], off offset:960
	ds_read_b128 v[10:13], v100
	ds_read_b128 v[14:17], v100 offset:1024
	ds_read_b128 v[148:151], v100 offset:2048
	ds_read_b128 v[152:155], v100 offset:3072
	ds_read_b128 v[156:159], v100 offset:4096
	ds_read_b128 v[162:165], v100 offset:5120
	s_waitcnt vmcnt(15) lgkmcnt(5)
	v_mfma_f32_16x16x32_bf16 v[10:13], v[2:5], v[10:13], 0
	s_waitcnt lgkmcnt(3)
	v_mfma_f32_16x16x32_bf16 v[148:151], v[2:5], v[148:151], 0
	s_waitcnt lgkmcnt(1)
	v_mfma_f32_16x16x32_bf16 v[156:159], v[2:5], v[156:159], 0
	v_mfma_f32_16x16x32_bf16 v[10:13], v[2:5], v[14:17], v[10:13]
	v_mfma_f32_16x16x32_bf16 v[14:17], v[2:5], v[152:155], v[148:151]
	s_nop 3
	ds_read_b128 v[148:151], v100 offset:6144
	ds_read_b128 v[152:155], v100 offset:7168
	s_waitcnt lgkmcnt(2)
	v_mfma_f32_16x16x32_bf16 v[2:5], v[2:5], v[162:165], v[156:159]
	s_waitcnt vmcnt(14) lgkmcnt(1)
	v_mfma_f32_16x16x32_bf16 v[10:13], v[6:9], v[148:151], v[10:13]
	ds_read_b128 v[148:151], v100 offset:8192
	ds_read_b128 v[156:159], v100 offset:9216
	s_waitcnt lgkmcnt(1)
	v_mfma_f32_16x16x32_bf16 v[14:17], v[6:9], v[148:151], v[14:17]
	ds_read_b128 v[148:151], v100 offset:10240
	ds_read_b128 v[162:165], v100 offset:11264
	s_waitcnt lgkmcnt(1)
	v_mfma_f32_16x16x32_bf16 v[2:5], v[6:9], v[148:151], v[2:5]
	s_nop 0
	v_mfma_f32_16x16x32_bf16 v[10:13], v[6:9], v[152:155], v[10:13]
	s_nop 0
	v_mfma_f32_16x16x32_bf16 v[14:17], v[6:9], v[156:159], v[14:17]
	s_waitcnt lgkmcnt(0)
	v_mfma_f32_16x16x32_bf16 v[2:5], v[6:9], v[162:165], v[2:5]
	ds_read_b128 v[6:9], v100 offset:12288
	ds_read_b128 v[156:159], v100 offset:13312
	s_waitcnt vmcnt(13) lgkmcnt(1)
	v_mfma_f32_16x16x32_bf16 v[6:9], v[170:173], v[6:9], v[10:13]
	s_nop 2
	ds_read_b128 v[10:13], v100 offset:14336
	ds_read_b128 v[162:165], v100 offset:15360
	s_waitcnt lgkmcnt(1)
	v_mfma_f32_16x16x32_bf16 v[10:13], v[170:173], v[10:13], v[14:17]
	s_nop 2
	ds_read_b128 v[14:17], v100 offset:16384
	ds_read_b128 v[166:169], v100 offset:17408
	s_waitcnt lgkmcnt(1)
	v_mfma_f32_16x16x32_bf16 v[2:5], v[170:173], v[14:17], v[2:5]
	v_mfma_f32_16x16x32_bf16 v[6:9], v[170:173], v[156:159], v[6:9]
	v_mfma_f32_16x16x32_bf16 v[10:13], v[170:173], v[162:165], v[10:13]
	s_waitcnt lgkmcnt(0)
	v_mfma_f32_16x16x32_bf16 v[2:5], v[170:173], v[166:169], v[2:5]
	ds_read_b128 v[14:17], v100 offset:18432
	ds_read_b128 v[148:151], v100 offset:19456
	s_waitcnt vmcnt(12) lgkmcnt(1)
	v_mfma_f32_16x16x32_bf16 v[6:9], v[174:177], v[14:17], v[6:9]
	ds_read_b128 v[14:17], v100 offset:20480
	ds_read_b128 v[156:159], v100 offset:21504
	s_waitcnt lgkmcnt(1)
	v_mfma_f32_16x16x32_bf16 v[10:13], v[174:177], v[14:17], v[10:13]
	ds_read_b128 v[14:17], v100 offset:22528
	ds_read_b128 v[162:165], v100 offset:23552
	s_waitcnt lgkmcnt(1)
	v_mfma_f32_16x16x32_bf16 v[2:5], v[174:177], v[14:17], v[2:5]
	s_nop 0
	v_mfma_f32_16x16x32_bf16 v[6:9], v[174:177], v[148:151], v[6:9]
	s_nop 0
	v_mfma_f32_16x16x32_bf16 v[10:13], v[174:177], v[156:159], v[10:13]
	s_waitcnt lgkmcnt(0)
	v_mfma_f32_16x16x32_bf16 v[2:5], v[174:177], v[162:165], v[2:5]
	ds_read_b128 v[152:155], v100 offset:24576
	ds_read_b128 v[156:159], v100 offset:25600
	s_waitcnt vmcnt(11) lgkmcnt(1)
	v_mfma_f32_16x16x32_bf16 v[6:9], v[178:181], v[152:155], v[6:9]
	ds_read_b128 v[152:155], v100 offset:26624
	ds_read_b128 v[162:165], v100 offset:27648
	s_waitcnt lgkmcnt(1)
	v_mfma_f32_16x16x32_bf16 v[10:13], v[178:181], v[152:155], v[10:13]
	ds_read_b128 v[152:155], v100 offset:28672
	ds_read_b128 v[166:169], v100 offset:29696
	s_waitcnt lgkmcnt(1)
	v_mfma_f32_16x16x32_bf16 v[2:5], v[178:181], v[152:155], v[2:5]
	v_mfma_f32_16x16x32_bf16 v[6:9], v[178:181], v[156:159], v[6:9]
	v_mfma_f32_16x16x32_bf16 v[10:13], v[178:181], v[162:165], v[10:13]
	s_waitcnt lgkmcnt(0)
	v_mfma_f32_16x16x32_bf16 v[2:5], v[178:181], v[166:169], v[2:5]
	ds_read_b128 v[14:17], v100 offset:30720
	ds_read_b128 v[152:155], v100 offset:31744
	s_waitcnt vmcnt(10) lgkmcnt(1)
	v_mfma_f32_16x16x32_bf16 v[6:9], v[184:187], v[14:17], v[6:9]
	ds_read_b128 v[14:17], v100 offset:32768
	ds_read_b128 v[156:159], v100 offset:33792
	s_waitcnt lgkmcnt(1)
	v_mfma_f32_16x16x32_bf16 v[10:13], v[184:187], v[14:17], v[10:13]
	s_nop 0
	v_mfma_f32_16x16x32_bf16 v[6:9], v[184:187], v[152:155], v[6:9]
	s_waitcnt lgkmcnt(0)
	v_mfma_f32_16x16x32_bf16 v[10:13], v[184:187], v[156:159], v[10:13]
	ds_read_b128 v[152:155], v100 offset:34816
	ds_read_b128 v[156:159], v100 offset:35840
	s_waitcnt lgkmcnt(1)
; #define LAS __attribute__((address_space(3)))
; __global__ void __launch_bounds__(512, 2) fwd(Args args) {
;     ...
;                     for (int kb = 0; kb < 16; ++kb) {
; #pragma unroll
;                         for (int n = 0; n < 3; ++n) { const LAS bf16x8* bp = (const LAS bf16x8*)(lds + ((kb * 3 + n) * 128 + lane) * 16);
;                             acc[n] = __builtin_amdgcn_mfma_f32_16x16x32_bf16(a[kb], bp[0], acc[n], 0, 0, 0); acc[n] = __builtin_amdgcn_mfma_f32_16x16x32_bf16(a[kb], bp[64], acc[n], 0, 0, 0); } }
	v_mfma_f32_16x16x32_bf16 v[2:5], v[184:187], v[152:155], v[2:5]
	s_nop 0
	s_waitcnt lgkmcnt(0)
	v_mfma_f32_16x16x32_bf16 v[2:5], v[184:187], v[156:159], v[2:5]
	ds_read_b128 v[148:151], v100 offset:36864
	ds_read_b128 v[156:159], v100 offset:37888
	s_waitcnt vmcnt(9) lgkmcnt(1)
	v_mfma_f32_16x16x32_bf16 v[6:9], v[188:191], v[148:151], v[6:9]
	s_waitcnt lgkmcnt(0)
	v_mfma_f32_16x16x32_bf16 v[6:9], v[188:191], v[156:159], v[6:9]
	ds_read_b128 v[148:151], v100 offset:38912
	ds_read_b128 v[156:159], v100 offset:39936
	s_waitcnt lgkmcnt(1)
	v_mfma_f32_16x16x32_bf16 v[10:13], v[188:191], v[148:151], v[10:13]
	s_waitcnt lgkmcnt(0)
	v_mfma_f32_16x16x32_bf16 v[10:13], v[188:191], v[156:159], v[10:13]
	ds_read_b128 v[148:151], v100 offset:40960
	ds_read_b128 v[156:159], v100 offset:41984
	s_waitcnt lgkmcnt(1)
	v_mfma_f32_16x16x32_bf16 v[2:5], v[188:191], v[148:151], v[2:5]
	s_waitcnt lgkmcnt(0)
	v_mfma_f32_16x16x32_bf16 v[2:5], v[188:191], v[156:159], v[2:5]
	ds_read_b128 v[14:17], v100 offset:43008
	ds_read_b128 v[148:151], v100 offset:44032
	s_waitcnt vmcnt(8) lgkmcnt(1)
	v_mfma_f32_16x16x32_bf16 v[6:9], v[202:205], v[14:17], v[6:9]
	s_waitcnt lgkmcnt(0)
	v_mfma_f32_16x16x32_bf16 v[6:9], v[202:205], v[148:151], v[6:9]
	ds_read_b128 v[14:17], v100 offset:45056
	ds_read_b128 v[148:151], v100 offset:46080
	s_waitcnt lgkmcnt(1)
	v_mfma_f32_16x16x32_bf16 v[10:13], v[202:205], v[14:17], v[10:13]
	s_nop 0
	s_waitcnt lgkmcnt(0)
	v_mfma_f32_16x16x32_bf16 v[10:13], v[202:205], v[148:151], v[10:13]
	ds_read_b128 v[148:151], v100 offset:47104
	ds_read_b128 v[156:159], v100 offset:48128
	s_waitcnt lgkmcnt(1)
	v_mfma_f32_16x16x32_bf16 v[2:5], v[202:205], v[148:151], v[2:5]
	s_nop 0
	s_waitcnt lgkmcnt(0)
	v_mfma_f32_16x16x32_bf16 v[2:5], v[202:205], v[156:159], v[2:5]
	ds_read_b128 v[152:155], v100 offset:49152
	ds_read_b128 v[156:159], v100 offset:50176
	s_waitcnt vmcnt(7) lgkmcnt(1)
	v_mfma_f32_16x16x32_bf16 v[6:9], v[206:209], v[152:155], v[6:9]
	s_waitcnt lgkmcnt(0)
	v_mfma_f32_16x16x32_bf16 v[6:9], v[206:209], v[156:159], v[6:9]
	ds_read_b128 v[152:155], v100 offset:51200
	ds_read_b128 v[156:159], v100 offset:52224
	s_waitcnt lgkmcnt(1)
	v_mfma_f32_16x16x32_bf16 v[10:13], v[206:209], v[152:155], v[10:13]
	s_waitcnt lgkmcnt(0)
	v_mfma_f32_16x16x32_bf16 v[10:13], v[206:209], v[156:159], v[10:13]
	ds_read_b128 v[152:155], v100 offset:53248
	ds_read_b128 v[156:159], v100 offset:54272
	s_waitcnt lgkmcnt(1)
	v_mfma_f32_16x16x32_bf16 v[2:5], v[206:209], v[152:155], v[2:5]
	s_waitcnt lgkmcnt(0)
	v_mfma_f32_16x16x32_bf16 v[2:5], v[206:209], v[156:159], v[2:5]
	ds_read_b128 v[14:17], v100 offset:55296
	ds_read_b128 v[152:155], v100 offset:56320
	s_waitcnt vmcnt(6) lgkmcnt(1)
	v_mfma_f32_16x16x32_bf16 v[6:9], v[214:217], v[14:17], v[6:9]
	s_waitcnt lgkmcnt(0)
	v_mfma_f32_16x16x32_bf16 v[6:9], v[214:217], v[152:155], v[6:9]
	ds_read_b128 v[14:17], v100 offset:57344
	ds_read_b128 v[152:155], v100 offset:58368
	s_waitcnt lgkmcnt(1)
	v_mfma_f32_16x16x32_bf16 v[10:13], v[214:217], v[14:17], v[10:13]
	s_nop 0
	s_waitcnt lgkmcnt(0)
	v_mfma_f32_16x16x32_bf16 v[10:13], v[214:217], v[152:155], v[10:13]
	ds_read_b128 v[152:155], v100 offset:59392
	ds_read_b128 v[156:159], v100 offset:60416
	s_waitcnt lgkmcnt(1)
	v_mfma_f32_16x16x32_bf16 v[2:5], v[214:217], v[152:155], v[2:5]
	s_nop 0
	s_waitcnt lgkmcnt(0)
	v_mfma_f32_16x16x32_bf16 v[2:5], v[214:217], v[156:159], v[2:5]
	ds_read_b128 v[148:151], v100 offset:61440
	ds_read_b128 v[156:159], v100 offset:62464
	s_waitcnt vmcnt(5) lgkmcnt(1)
	v_mfma_f32_16x16x32_bf16 v[6:9], v[218:221], v[148:151], v[6:9]
	s_waitcnt lgkmcnt(0)
	v_mfma_f32_16x16x32_bf16 v[6:9], v[218:221], v[156:159], v[6:9]
	ds_read_b128 v[148:151], v100 offset:63488
	ds_read_b128 v[156:159], v100 offset:64512
	s_waitcnt lgkmcnt(1)
	v_mfma_f32_16x16x32_bf16 v[10:13], v[218:221], v[148:151], v[10:13]
	s_waitcnt lgkmcnt(0)
	v_mfma_f32_16x16x32_bf16 v[10:13], v[218:221], v[156:159], v[10:13]
	ds_read_b128 v[148:151], v114
	ds_read_b128 v[156:159], v115
	s_waitcnt lgkmcnt(1)
	v_mfma_f32_16x16x32_bf16 v[2:5], v[218:221], v[148:151], v[2:5]
	s_waitcnt lgkmcnt(0)
	v_mfma_f32_16x16x32_bf16 v[2:5], v[218:221], v[156:159], v[2:5]
	ds_read_b128 v[14:17], v116
	ds_read_b128 v[148:151], v117
	s_waitcnt vmcnt(4) lgkmcnt(1)
	v_mfma_f32_16x16x32_bf16 v[6:9], v[222:225], v[14:17], v[6:9]
	s_waitcnt lgkmcnt(0)
	v_mfma_f32_16x16x32_bf16 v[6:9], v[222:225], v[148:151], v[6:9]
	ds_read_b128 v[14:17], v118
	ds_read_b128 v[148:151], v119
	s_waitcnt lgkmcnt(1)
	v_mfma_f32_16x16x32_bf16 v[10:13], v[222:225], v[14:17], v[10:13]
	s_nop 0
	s_waitcnt lgkmcnt(0)
	v_mfma_f32_16x16x32_bf16 v[10:13], v[222:225], v[148:151], v[10:13]
	ds_read_b128 v[148:151], v120
	ds_read_b128 v[156:159], v121
	s_waitcnt lgkmcnt(1)
	v_mfma_f32_16x16x32_bf16 v[2:5], v[222:225], v[148:151], v[2:5]
	s_nop 0
	s_waitcnt lgkmcnt(0)
	v_mfma_f32_16x16x32_bf16 v[2:5], v[222:225], v[156:159], v[2:5]
	ds_read_b128 v[152:155], v122
	ds_read_b128 v[156:159], v123
	s_waitcnt vmcnt(3) lgkmcnt(1)
	v_mfma_f32_16x16x32_bf16 v[6:9], v[226:229], v[152:155], v[6:9]
	s_waitcnt lgkmcnt(0)
	v_mfma_f32_16x16x32_bf16 v[6:9], v[226:229], v[156:159], v[6:9]
	ds_read_b128 v[152:155], v124
	ds_read_b128 v[156:159], v125
	s_waitcnt lgkmcnt(1)
	v_mfma_f32_16x16x32_bf16 v[10:13], v[226:229], v[152:155], v[10:13]
	s_waitcnt lgkmcnt(0)
	v_mfma_f32_16x16x32_bf16 v[10:13], v[226:229], v[156:159], v[10:13]
	ds_read_b128 v[152:155], v126
	ds_read_b128 v[156:159], v127
	s_waitcnt lgkmcnt(1)
	v_mfma_f32_16x16x32_bf16 v[2:5], v[226:229], v[152:155], v[2:5]
	s_waitcnt lgkmcnt(0)
; #define LAS __attribute__((address_space(3)))
; #define LDS_WAIT() asm volatile("s_waitcnt lgkmcnt(0)" ::: "memory")
; __global__ void __launch_bounds__(512, 2) fwd(Args args) {
;     ...
;                     for (int kb = 0; kb < 32; ++kb) a[kb] = *(const bf16x8*)(xr + kb * 32);
; #pragma unroll
;                     for (int kb = 0; kb < 16; ++kb) {
; #pragma unroll
;                         for (int n = 0; n < 3; ++n) { const LAS bf16x8* bp = (const LAS bf16x8*)(lds + ((kb * 3 + n) * 128 + lane) * 16);
;                             acc[n] = __builtin_amdgcn_mfma_f32_16x16x32_bf16(a[kb], bp[0], acc[n], 0, 0, 0); acc[n] = __builtin_amdgcn_mfma_f32_16x16x32_bf16(a[kb], bp[64], acc[n], 0, 0, 0); } }
;                     LDS_WAIT(); asm volatile("" ::: "memory"); __builtin_amdgcn_s_barrier(); asm volatile("" ::: "memory");
;                     __builtin_amdgcn_s_barrier(); asm volatile("" ::: "memory");
; #pragma unroll
;                     for (int kb = 0; kb < 16; ++kb) {
; #pragma unroll
;                         for (int n = 0; n < 3; ++n) { const LAS bf16x8* bp = (const LAS bf16x8*)(lds + ((kb * 3 + n) * 128 + lane) * 16);
;                             acc[n] = __builtin_amdgcn_mfma_f32_16x16x32_bf16(a[16 + kb], bp[0], acc[n], 0, 0, 0); acc[n] = __builtin_amdgcn_mfma_f32_16x16x32_bf16(a[16 + kb], bp[64], acc[n], 0, 0, 0); } }
	v_mfma_f32_16x16x32_bf16 v[2:5], v[226:229], v[156:159], v[2:5]
	ds_read_b128 v[14:17], v128
	ds_read_b128 v[152:155], v129
	s_waitcnt vmcnt(2) lgkmcnt(1)
	v_mfma_f32_16x16x32_bf16 v[6:9], v[232:235], v[14:17], v[6:9]
	s_waitcnt lgkmcnt(0)
	v_mfma_f32_16x16x32_bf16 v[6:9], v[232:235], v[152:155], v[6:9]
	ds_read_b128 v[14:17], v130
	ds_read_b128 v[152:155], v131
	s_waitcnt lgkmcnt(1)
	v_mfma_f32_16x16x32_bf16 v[10:13], v[232:235], v[14:17], v[10:13]
	s_nop 0
	s_waitcnt lgkmcnt(0)
	v_mfma_f32_16x16x32_bf16 v[10:13], v[232:235], v[152:155], v[10:13]
	ds_read_b128 v[152:155], v132
	ds_read_b128 v[156:159], v133
	s_waitcnt lgkmcnt(1)
	v_mfma_f32_16x16x32_bf16 v[2:5], v[232:235], v[152:155], v[2:5]
	s_nop 0
	s_waitcnt lgkmcnt(0)
	v_mfma_f32_16x16x32_bf16 v[2:5], v[232:235], v[156:159], v[2:5]
	ds_read_b128 v[148:151], v134
	ds_read_b128 v[156:159], v135
	s_waitcnt vmcnt(1) lgkmcnt(1)
	v_mfma_f32_16x16x32_bf16 v[6:9], v[238:241], v[148:151], v[6:9]
	s_waitcnt lgkmcnt(0)
	v_mfma_f32_16x16x32_bf16 v[6:9], v[238:241], v[156:159], v[6:9]
	ds_read_b128 v[148:151], v136
	ds_read_b128 v[156:159], v137
	s_waitcnt lgkmcnt(1)
	v_mfma_f32_16x16x32_bf16 v[10:13], v[238:241], v[148:151], v[10:13]
	global_load_dwordx4 v[148:151], v[0:1], off offset:1024
	s_waitcnt lgkmcnt(0)
	v_mfma_f32_16x16x32_bf16 v[10:13], v[238:241], v[156:159], v[10:13]
	ds_read_b128 v[156:159], v138
	ds_read_b128 v[162:165], v139
	ds_read_b128 v[166:169], v140
	s_waitcnt lgkmcnt(2)
	v_mfma_f32_16x16x32_bf16 v[2:5], v[238:241], v[156:159], v[2:5]
	global_load_dwordx4 v[156:159], v[0:1], off offset:1088
	s_waitcnt lgkmcnt(1)
	v_mfma_f32_16x16x32_bf16 v[2:5], v[238:241], v[162:165], v[2:5]
	global_load_dwordx4 v[162:165], v[0:1], off offset:1152
	global_load_dwordx4 v[170:173], v[0:1], off offset:1216
	ds_read_b128 v[14:17], v141
	s_waitcnt vmcnt(4) lgkmcnt(1)
	v_mfma_f32_16x16x32_bf16 v[6:9], v[242:245], v[166:169], v[6:9]
	global_load_dwordx4 v[166:169], v[0:1], off offset:1280
	global_load_dwordx4 v[174:177], v[0:1], off offset:1344
	ds_read_b128 v[178:181], v142
	global_load_dwordx4 v[186:189], v[0:1], off offset:1408
	global_load_dwordx4 v[190:193], v[0:1], off offset:1472
	s_waitcnt lgkmcnt(1)
	v_mfma_f32_16x16x32_bf16 v[182:185], v[242:245], v[14:17], v[6:9]
	s_nop 2
	ds_read_b128 v[6:9], v143
	s_waitcnt lgkmcnt(1)
	v_mfma_f32_16x16x32_bf16 v[10:13], v[242:245], v[178:181], v[10:13]
	global_load_dwordx4 v[178:181], v[0:1], off offset:1536
	global_load_dwordx4 v[196:199], v[0:1], off offset:1600
	ds_read_b128 v[200:203], v144
	global_load_dwordx4 v[208:211], v[0:1], off offset:1664
	global_load_dwordx4 v[16:19], v[0:1], off offset:1728
	ds_read_b128 v[214:217], v145
	s_waitcnt lgkmcnt(1)
	v_mfma_f32_16x16x32_bf16 v[200:203], v[242:245], v[200:203], v[2:5]
	v_mfma_f32_16x16x32_bf16 v[204:207], v[242:245], v[6:9], v[10:13]
	s_nop 2
	global_load_dwordx4 v[12:15], v[0:1], off offset:1792
	global_load_dwordx4 v[8:11], v[0:1], off offset:1856
	global_load_dwordx4 v[4:7], v[0:1], off offset:1920
	s_nop 0
	global_load_dwordx4 v[0:3], v[0:1], off offset:1984
	s_waitcnt lgkmcnt(0)
	s_barrier
	s_barrier
	s_waitcnt lgkmcnt(0)
	v_mfma_f32_16x16x32_bf16 v[152:155], v[242:245], v[214:217], v[200:203]
	s_nop 2
	ds_read_b128 v[200:203], v100
	ds_read_b128 v[214:217], v100 offset:1024
	s_waitcnt vmcnt(15) lgkmcnt(1)
	v_mfma_f32_16x16x32_bf16 v[182:185], v[148:151], v[200:203], v[182:185]
	s_waitcnt lgkmcnt(0)
	v_mfma_f32_16x16x32_bf16 v[182:185], v[148:151], v[214:217], v[182:185]
	ds_read_b128 v[200:203], v100 offset:2048
	ds_read_b128 v[214:217], v100 offset:3072
	s_waitcnt lgkmcnt(1)
	v_mfma_f32_16x16x32_bf16 v[200:203], v[148:151], v[200:203], v[204:207]
	s_waitcnt lgkmcnt(0)
	v_mfma_f32_16x16x32_bf16 v[200:203], v[148:151], v[214:217], v[200:203]
	s_nop 0
	ds_read_b128 v[204:207], v100 offset:4096
	ds_read_b128 v[214:217], v100 offset:5120
	s_waitcnt lgkmcnt(1)
	v_mfma_f32_16x16x32_bf16 v[152:155], v[148:151], v[204:207], v[152:155]
	s_waitcnt lgkmcnt(0)
	v_mfma_f32_16x16x32_bf16 v[148:151], v[148:151], v[214:217], v[152:155]
	s_nop 5
	ds_read_b128 v[152:155], v100 offset:6144
	ds_read_b128 v[204:207], v100 offset:7168
	s_waitcnt vmcnt(14) lgkmcnt(1)
	v_mfma_f32_16x16x32_bf16 v[152:155], v[156:159], v[152:155], v[182:185]
	s_waitcnt lgkmcnt(0)
	v_mfma_f32_16x16x32_bf16 v[152:155], v[156:159], v[204:207], v[152:155]
	s_nop 0
	ds_read_b128 v[182:185], v100 offset:8192
	ds_read_b128 v[204:207], v100 offset:9216
	s_waitcnt lgkmcnt(1)
	v_mfma_f32_16x16x32_bf16 v[182:185], v[156:159], v[182:185], v[200:203]
	s_waitcnt lgkmcnt(0)
	v_mfma_f32_16x16x32_bf16 v[182:185], v[156:159], v[204:207], v[182:185]
	s_nop 0
	ds_read_b128 v[200:203], v100 offset:10240
	ds_read_b128 v[204:207], v100 offset:11264
	s_waitcnt lgkmcnt(1)
	v_mfma_f32_16x16x32_bf16 v[148:151], v[156:159], v[200:203], v[148:151]
	s_waitcnt lgkmcnt(0)
	v_mfma_f32_16x16x32_bf16 v[148:151], v[156:159], v[204:207], v[148:151]
	ds_read_b128 v[156:159], v100 offset:12288
	ds_read_b128 v[200:203], v100 offset:13312
	s_waitcnt vmcnt(13) lgkmcnt(1)
	v_mfma_f32_16x16x32_bf16 v[152:155], v[162:165], v[156:159], v[152:155]
	s_waitcnt lgkmcnt(0)
	v_mfma_f32_16x16x32_bf16 v[152:155], v[162:165], v[200:203], v[152:155]
	ds_read_b128 v[156:159], v100 offset:14336
	ds_read_b128 v[200:203], v100 offset:15360
	s_waitcnt lgkmcnt(1)
	v_mfma_f32_16x16x32_bf16 v[156:159], v[162:165], v[156:159], v[182:185]
	s_waitcnt lgkmcnt(0)
	v_mfma_f32_16x16x32_bf16 v[156:159], v[162:165], v[200:203], v[156:159]
	s_nop 0
	ds_read_b128 v[182:185], v100 offset:16384
	ds_read_b128 v[200:203], v100 offset:17408
	s_waitcnt lgkmcnt(1)
; #define LAS __attribute__((address_space(3)))
; #define LDS_WAIT() asm volatile("s_waitcnt lgkmcnt(0)" ::: "memory")
; __global__ void __launch_bounds__(512, 2) fwd(Args args) {
;     ...
;                     for (int kb = 0; kb < 32; ++kb) a[kb] = *(const bf16x8*)(xr + kb * 32);
; #pragma unroll
;                     for (int kb = 0; kb < 16; ++kb) {
; #pragma unroll
;                         for (int n = 0; n < 3; ++n) { const LAS bf16x8* bp = (const LAS bf16x8*)(lds + ((kb * 3 + n) * 128 + lane) * 16);
;                             acc[n] = __builtin_amdgcn_mfma_f32_16x16x32_bf16(a[kb], bp[0], acc[n], 0, 0, 0); acc[n] = __builtin_amdgcn_mfma_f32_16x16x32_bf16(a[kb], bp[64], acc[n], 0, 0, 0); } }
;                     LDS_WAIT(); asm volatile("" ::: "memory"); __builtin_amdgcn_s_barrier(); asm volatile("" ::: "memory");
;                     __builtin_amdgcn_s_barrier(); asm volatile("" ::: "memory");
; #pragma unroll
;                     for (int kb = 0; kb < 16; ++kb) {
; #pragma unroll
;                         for (int n = 0; n < 3; ++n) { const LAS bf16x8* bp = (const LAS bf16x8*)(lds + ((kb * 3 + n) * 128 + lane) * 16);
;                             acc[n] = __builtin_amdgcn_mfma_f32_16x16x32_bf16(a[16 + kb], bp[0], acc[n], 0, 0, 0); acc[n] = __builtin_amdgcn_mfma_f32_16x16x32_bf16(a[16 + kb], bp[64], acc[n], 0, 0, 0); } }
	v_mfma_f32_16x16x32_bf16 v[148:151], v[162:165], v[182:185], v[148:151]
	s_waitcnt lgkmcnt(0)
	v_mfma_f32_16x16x32_bf16 v[148:151], v[162:165], v[200:203], v[148:151]
	ds_read_b128 v[162:165], v100 offset:18432
	ds_read_b128 v[182:185], v100 offset:19456
	s_waitcnt vmcnt(12) lgkmcnt(1)
	v_mfma_f32_16x16x32_bf16 v[152:155], v[170:173], v[162:165], v[152:155]
	s_waitcnt lgkmcnt(0)
	v_mfma_f32_16x16x32_bf16 v[152:155], v[170:173], v[182:185], v[152:155]
	ds_read_b128 v[162:165], v100 offset:20480
	ds_read_b128 v[182:185], v100 offset:21504
	s_waitcnt lgkmcnt(1)
	v_mfma_f32_16x16x32_bf16 v[156:159], v[170:173], v[162:165], v[156:159]
	s_waitcnt lgkmcnt(0)
	v_mfma_f32_16x16x32_bf16 v[156:159], v[170:173], v[182:185], v[156:159]
	ds_read_b128 v[162:165], v100 offset:22528
	ds_read_b128 v[182:185], v100 offset:23552
	s_waitcnt lgkmcnt(1)
	v_mfma_f32_16x16x32_bf16 v[148:151], v[170:173], v[162:165], v[148:151]
	s_waitcnt lgkmcnt(0)
	v_mfma_f32_16x16x32_bf16 v[148:151], v[170:173], v[182:185], v[148:151]
	ds_read_b128 v[162:165], v100 offset:24576
	ds_read_b128 v[170:173], v100 offset:25600
	s_waitcnt vmcnt(11) lgkmcnt(1)
	v_mfma_f32_16x16x32_bf16 v[152:155], v[166:169], v[162:165], v[152:155]
	s_waitcnt lgkmcnt(0)
	v_mfma_f32_16x16x32_bf16 v[152:155], v[166:169], v[170:173], v[152:155]
	ds_read_b128 v[162:165], v100 offset:26624
	ds_read_b128 v[170:173], v100 offset:27648
	s_waitcnt lgkmcnt(1)
	v_mfma_f32_16x16x32_bf16 v[156:159], v[166:169], v[162:165], v[156:159]
	s_waitcnt lgkmcnt(0)
	v_mfma_f32_16x16x32_bf16 v[156:159], v[166:169], v[170:173], v[156:159]
	ds_read_b128 v[162:165], v100 offset:28672
	ds_read_b128 v[170:173], v100 offset:29696
	s_waitcnt lgkmcnt(1)
	v_mfma_f32_16x16x32_bf16 v[148:151], v[166:169], v[162:165], v[148:151]
	s_waitcnt lgkmcnt(0)
	v_mfma_f32_16x16x32_bf16 v[148:151], v[166:169], v[170:173], v[148:151]
	ds_read_b128 v[162:165], v100 offset:30720
	ds_read_b128 v[166:169], v100 offset:31744
	s_waitcnt vmcnt(10) lgkmcnt(1)
	v_mfma_f32_16x16x32_bf16 v[152:155], v[174:177], v[162:165], v[152:155]
	s_waitcnt lgkmcnt(0)
	v_mfma_f32_16x16x32_bf16 v[152:155], v[174:177], v[166:169], v[152:155]
	ds_read_b128 v[162:165], v100 offset:32768
	ds_read_b128 v[166:169], v100 offset:33792
	s_waitcnt lgkmcnt(1)
	v_mfma_f32_16x16x32_bf16 v[156:159], v[174:177], v[162:165], v[156:159]
	s_waitcnt lgkmcnt(0)
	v_mfma_f32_16x16x32_bf16 v[156:159], v[174:177], v[166:169], v[156:159]
	ds_read_b128 v[162:165], v100 offset:34816
	ds_read_b128 v[166:169], v100 offset:35840
	s_waitcnt lgkmcnt(1)
	v_mfma_f32_16x16x32_bf16 v[148:151], v[174:177], v[162:165], v[148:151]
	s_waitcnt lgkmcnt(0)
	v_mfma_f32_16x16x32_bf16 v[148:151], v[174:177], v[166:169], v[148:151]
	ds_read_b128 v[162:165], v100 offset:36864
	ds_read_b128 v[166:169], v100 offset:37888
	s_waitcnt vmcnt(9) lgkmcnt(1)
	v_mfma_f32_16x16x32_bf16 v[152:155], v[186:189], v[162:165], v[152:155]
	s_waitcnt lgkmcnt(0)
	v_mfma_f32_16x16x32_bf16 v[152:155], v[186:189], v[166:169], v[152:155]
	ds_read_b128 v[162:165], v100 offset:38912
	ds_read_b128 v[166:169], v100 offset:39936
	s_waitcnt lgkmcnt(1)
	v_mfma_f32_16x16x32_bf16 v[156:159], v[186:189], v[162:165], v[156:159]
	s_waitcnt lgkmcnt(0)
	v_mfma_f32_16x16x32_bf16 v[156:159], v[186:189], v[166:169], v[156:159]
	ds_read_b128 v[162:165], v100 offset:40960
	ds_read_b128 v[166:169], v100 offset:41984
	s_waitcnt lgkmcnt(1)
	v_mfma_f32_16x16x32_bf16 v[148:151], v[186:189], v[162:165], v[148:151]
	s_waitcnt lgkmcnt(0)
	v_mfma_f32_16x16x32_bf16 v[148:151], v[186:189], v[166:169], v[148:151]
	ds_read_b128 v[162:165], v100 offset:43008
	ds_read_b128 v[166:169], v100 offset:44032
	s_waitcnt vmcnt(8) lgkmcnt(1)
	v_mfma_f32_16x16x32_bf16 v[152:155], v[190:193], v[162:165], v[152:155]
	s_waitcnt lgkmcnt(0)
	v_mfma_f32_16x16x32_bf16 v[152:155], v[190:193], v[166:169], v[152:155]
	ds_read_b128 v[162:165], v100 offset:45056
	ds_read_b128 v[166:169], v100 offset:46080
	s_waitcnt lgkmcnt(1)
	v_mfma_f32_16x16x32_bf16 v[156:159], v[190:193], v[162:165], v[156:159]
	s_waitcnt lgkmcnt(0)
	v_mfma_f32_16x16x32_bf16 v[156:159], v[190:193], v[166:169], v[156:159]
	ds_read_b128 v[162:165], v100 offset:47104
	ds_read_b128 v[166:169], v100 offset:48128
	s_waitcnt lgkmcnt(1)
	v_mfma_f32_16x16x32_bf16 v[148:151], v[190:193], v[162:165], v[148:151]
	s_waitcnt lgkmcnt(0)
	v_mfma_f32_16x16x32_bf16 v[148:151], v[190:193], v[166:169], v[148:151]
	ds_read_b128 v[162:165], v100 offset:49152
	ds_read_b128 v[166:169], v100 offset:50176
	s_waitcnt vmcnt(7) lgkmcnt(1)
	v_mfma_f32_16x16x32_bf16 v[152:155], v[178:181], v[162:165], v[152:155]
	s_waitcnt lgkmcnt(0)
	v_mfma_f32_16x16x32_bf16 v[152:155], v[178:181], v[166:169], v[152:155]
	ds_read_b128 v[162:165], v100 offset:51200
	ds_read_b128 v[166:169], v100 offset:52224
	s_waitcnt lgkmcnt(1)
	v_mfma_f32_16x16x32_bf16 v[156:159], v[178:181], v[162:165], v[156:159]
	s_waitcnt lgkmcnt(0)
	v_mfma_f32_16x16x32_bf16 v[156:159], v[178:181], v[166:169], v[156:159]
	ds_read_b128 v[162:165], v100 offset:53248
	ds_read_b128 v[166:169], v100 offset:54272
	s_waitcnt lgkmcnt(1)
	v_mfma_f32_16x16x32_bf16 v[148:151], v[178:181], v[162:165], v[148:151]
	s_waitcnt lgkmcnt(0)
	v_mfma_f32_16x16x32_bf16 v[148:151], v[178:181], v[166:169], v[148:151]
	ds_read_b128 v[162:165], v100 offset:55296
	ds_read_b128 v[166:169], v100 offset:56320
	s_waitcnt vmcnt(6) lgkmcnt(1)
	v_mfma_f32_16x16x32_bf16 v[152:155], v[196:199], v[162:165], v[152:155]
	s_waitcnt lgkmcnt(0)
; #define LAS __attribute__((address_space(3)))
; #define LDS_WAIT() asm volatile("s_waitcnt lgkmcnt(0)" ::: "memory")
; __global__ void __launch_bounds__(512, 2) fwd(Args args) {
;     ...
;                     for (int kb = 0; kb < 16; ++kb) {
; #pragma unroll
;                         for (int n = 0; n < 3; ++n) { const LAS bf16x8* bp = (const LAS bf16x8*)(lds + ((kb * 3 + n) * 128 + lane) * 16);
;                             acc[n] = __builtin_amdgcn_mfma_f32_16x16x32_bf16(a[kb], bp[0], acc[n], 0, 0, 0); acc[n] = __builtin_amdgcn_mfma_f32_16x16x32_bf16(a[kb], bp[64], acc[n], 0, 0, 0); } }
;                     LDS_WAIT(); asm volatile("" ::: "memory"); __builtin_amdgcn_s_barrier(); asm volatile("" ::: "memory");
;                     __builtin_amdgcn_s_barrier(); asm volatile("" ::: "memory");
; #pragma unroll
;                     for (int kb = 0; kb < 16; ++kb) {
; #pragma unroll
;                         for (int n = 0; n < 3; ++n) { const LAS bf16x8* bp = (const LAS bf16x8*)(lds + ((kb * 3 + n) * 128 + lane) * 16);
;                             acc[n] = __builtin_amdgcn_mfma_f32_16x16x32_bf16(a[16 + kb], bp[0], acc[n], 0, 0, 0); acc[n] = __builtin_amdgcn_mfma_f32_16x16x32_bf16(a[16 + kb], bp[64], acc[n], 0, 0, 0); } }
; #pragma unroll
;                     for (int n = 0; n < 3; ++n) {
; #pragma unroll
;                         for (int q = 0; q < 4; ++q) lg[(wave * 16 + (lane >> 4) * 4 + q) * 49 + n * 16 + (lane & 15)] = acc[n][q]; }
	v_mfma_f32_16x16x32_bf16 v[152:155], v[196:199], v[166:169], v[152:155]
	ds_read_b128 v[162:165], v100 offset:57344
	ds_read_b128 v[166:169], v100 offset:58368
	s_waitcnt lgkmcnt(1)
	v_mfma_f32_16x16x32_bf16 v[156:159], v[196:199], v[162:165], v[156:159]
	s_waitcnt lgkmcnt(0)
	v_mfma_f32_16x16x32_bf16 v[156:159], v[196:199], v[166:169], v[156:159]
	ds_read_b128 v[162:165], v100 offset:59392
	ds_read_b128 v[166:169], v100 offset:60416
	s_waitcnt lgkmcnt(1)
	v_mfma_f32_16x16x32_bf16 v[148:151], v[196:199], v[162:165], v[148:151]
	s_waitcnt lgkmcnt(0)
	v_mfma_f32_16x16x32_bf16 v[148:151], v[196:199], v[166:169], v[148:151]
	ds_read_b128 v[162:165], v100 offset:61440
	ds_read_b128 v[166:169], v100 offset:62464
	s_waitcnt vmcnt(5) lgkmcnt(1)
	v_mfma_f32_16x16x32_bf16 v[152:155], v[208:211], v[162:165], v[152:155]
	s_waitcnt lgkmcnt(0)
	v_mfma_f32_16x16x32_bf16 v[152:155], v[208:211], v[166:169], v[152:155]
	ds_read_b128 v[162:165], v100 offset:63488
	ds_read_b128 v[166:169], v100 offset:64512
	s_waitcnt lgkmcnt(1)
	v_mfma_f32_16x16x32_bf16 v[156:159], v[208:211], v[162:165], v[156:159]
	s_waitcnt lgkmcnt(0)
	v_mfma_f32_16x16x32_bf16 v[156:159], v[208:211], v[166:169], v[156:159]
	ds_read_b128 v[162:165], v114
	ds_read_b128 v[166:169], v115
	s_waitcnt lgkmcnt(1)
	v_mfma_f32_16x16x32_bf16 v[148:151], v[208:211], v[162:165], v[148:151]
	s_waitcnt lgkmcnt(0)
	v_mfma_f32_16x16x32_bf16 v[148:151], v[208:211], v[166:169], v[148:151]
	ds_read_b128 v[162:165], v116
	ds_read_b128 v[166:169], v117
	s_waitcnt vmcnt(4) lgkmcnt(1)
	v_mfma_f32_16x16x32_bf16 v[152:155], v[16:19], v[162:165], v[152:155]
	s_waitcnt lgkmcnt(0)
	v_mfma_f32_16x16x32_bf16 v[152:155], v[16:19], v[166:169], v[152:155]
	ds_read_b128 v[162:165], v118
	ds_read_b128 v[166:169], v119
	s_waitcnt lgkmcnt(1)
	v_mfma_f32_16x16x32_bf16 v[156:159], v[16:19], v[162:165], v[156:159]
	s_waitcnt lgkmcnt(0)
	v_mfma_f32_16x16x32_bf16 v[156:159], v[16:19], v[166:169], v[156:159]
	ds_read_b128 v[162:165], v120
	ds_read_b128 v[166:169], v121
	s_waitcnt lgkmcnt(1)
	v_mfma_f32_16x16x32_bf16 v[148:151], v[16:19], v[162:165], v[148:151]
	s_waitcnt lgkmcnt(0)
	v_mfma_f32_16x16x32_bf16 v[16:19], v[16:19], v[166:169], v[148:151]
	s_nop 5
	ds_read_b128 v[148:151], v122
	ds_read_b128 v[162:165], v123
	s_waitcnt vmcnt(3) lgkmcnt(1)
	v_mfma_f32_16x16x32_bf16 v[148:151], v[12:15], v[148:151], v[152:155]
	s_waitcnt lgkmcnt(0)
	v_mfma_f32_16x16x32_bf16 v[148:151], v[12:15], v[162:165], v[148:151]
	s_nop 0
	ds_read_b128 v[152:155], v124
	ds_read_b128 v[162:165], v125
	s_waitcnt lgkmcnt(1)
	v_mfma_f32_16x16x32_bf16 v[152:155], v[12:15], v[152:155], v[156:159]
	s_waitcnt lgkmcnt(0)
	v_mfma_f32_16x16x32_bf16 v[152:155], v[12:15], v[162:165], v[152:155]
	s_nop 0
	ds_read_b128 v[156:159], v126
	ds_read_b128 v[162:165], v127
	s_waitcnt lgkmcnt(1)
	v_mfma_f32_16x16x32_bf16 v[16:19], v[12:15], v[156:159], v[16:19]
	s_waitcnt lgkmcnt(0)
	v_mfma_f32_16x16x32_bf16 v[12:15], v[12:15], v[162:165], v[16:19]
	s_nop 5
	ds_read_b128 v[16:19], v128
	ds_read_b128 v[156:159], v129
	s_waitcnt vmcnt(2) lgkmcnt(1)
	v_mfma_f32_16x16x32_bf16 v[16:19], v[8:11], v[16:19], v[148:151]
	s_waitcnt lgkmcnt(0)
	v_mfma_f32_16x16x32_bf16 v[16:19], v[8:11], v[156:159], v[16:19]
	s_nop 0
	ds_read_b128 v[148:151], v130
	ds_read_b128 v[156:159], v131
	s_waitcnt lgkmcnt(1)
	v_mfma_f32_16x16x32_bf16 v[148:151], v[8:11], v[148:151], v[152:155]
	s_waitcnt lgkmcnt(0)
	v_mfma_f32_16x16x32_bf16 v[148:151], v[8:11], v[156:159], v[148:151]
	s_nop 0
	ds_read_b128 v[152:155], v132
	ds_read_b128 v[156:159], v133
	s_waitcnt lgkmcnt(1)
	v_mfma_f32_16x16x32_bf16 v[12:15], v[8:11], v[152:155], v[12:15]
	s_waitcnt lgkmcnt(0)
	v_mfma_f32_16x16x32_bf16 v[8:11], v[8:11], v[156:159], v[12:15]
	s_nop 5
	ds_read_b128 v[12:15], v134
	ds_read_b128 v[152:155], v135
	s_waitcnt vmcnt(1) lgkmcnt(1)
	v_mfma_f32_16x16x32_bf16 v[12:15], v[4:7], v[12:15], v[16:19]
	s_waitcnt lgkmcnt(0)
	v_mfma_f32_16x16x32_bf16 v[12:15], v[4:7], v[152:155], v[12:15]
	s_nop 0
	ds_read_b128 v[16:19], v136
	ds_read_b128 v[152:155], v137
	s_waitcnt lgkmcnt(1)
	v_mfma_f32_16x16x32_bf16 v[16:19], v[4:7], v[16:19], v[148:151]
	s_waitcnt lgkmcnt(0)
	v_mfma_f32_16x16x32_bf16 v[16:19], v[4:7], v[152:155], v[16:19]
	s_nop 0
	ds_read_b128 v[148:151], v138
	ds_read_b128 v[152:155], v139
	s_waitcnt lgkmcnt(1)
	v_mfma_f32_16x16x32_bf16 v[8:11], v[4:7], v[148:151], v[8:11]
	s_waitcnt lgkmcnt(0)
	v_mfma_f32_16x16x32_bf16 v[4:7], v[4:7], v[152:155], v[8:11]
	s_nop 5
	ds_read_b128 v[8:11], v140
	ds_read_b128 v[148:151], v141
	s_waitcnt vmcnt(0) lgkmcnt(1)
	v_mfma_f32_16x16x32_bf16 v[8:11], v[0:3], v[8:11], v[12:15]
	s_waitcnt lgkmcnt(0)
	v_mfma_f32_16x16x32_bf16 v[8:11], v[0:3], v[148:151], v[8:11]
	s_nop 0
	ds_read_b128 v[12:15], v142
	ds_read_b128 v[148:151], v143
	s_waitcnt lgkmcnt(1)
	v_mfma_f32_16x16x32_bf16 v[12:15], v[0:3], v[12:15], v[16:19]
	s_waitcnt lgkmcnt(0)
	v_mfma_f32_16x16x32_bf16 v[12:15], v[0:3], v[148:151], v[12:15]
	s_nop 0
	ds_read_b128 v[16:19], v144
	ds_read_b128 v[148:151], v145
	s_nop 4
	ds_write2_b32 v146, v8, v12 offset1:16
	ds_write2_b32 v146, v10, v14 offset0:98 offset1:114
	s_waitcnt lgkmcnt(3)
	v_mfma_f32_16x16x32_bf16 v[4:7], v[0:3], v[16:19], v[4:7]
	s_waitcnt lgkmcnt(2)
	v_mfma_f32_16x16x32_bf16 v[0:3], v[0:3], v[148:151], v[4:7]
	s_nop 7
	ds_write2_b32 v146, v0, v9 offset0:32 offset1:49
	ds_write2_b32 v146, v13, v1 offset0:65 offset1:81
	ds_write2_b32 v146, v2, v11 offset0:130 offset1:147
	ds_write2_b32 v146, v15, v3 offset0:163 offset1:179
